# selection: compact rank loop over ambiguous chunks only (replaces 64-iteration compiler code); 8 KiB code warm-up
# speedup vs baseline: 1.0021x; 1.0021x over previous
.Lrg_slow:
	s_getpc_b64 s[4:5]
	s_and_b32 s4, s4, -16
	v_lshlrev_b32_e32 v2, 4, v1
	global_load_dwordx4 v[100:103], v2, s[4:5] offset:0
	global_load_dwordx4 v[104:107], v2, s[4:5] offset:1024
	global_load_dwordx4 v[108:111], v2, s[4:5] offset:2048
	global_load_dwordx4 v[112:115], v2, s[4:5] offset:3072
	s_add_u32 s4, s4, 0x1000
	s_addc_u32 s5, s5, 0
	global_load_dwordx4 v[116:119], v2, s[4:5] offset:0
	global_load_dwordx4 v[120:123], v2, s[4:5] offset:1024
	global_load_dwordx4 v[124:127], v2, s[4:5] offset:2048
	global_load_dwordx4 v[128:131], v2, s[4:5] offset:3072
	s_add_u32 s4, s4, 0x1000
	s_addc_u32 s5, s5, 0
	s_mov_b32 s3, s24
	s_mov_b32 s33, s27
	v_mov_b32_e32 v26, v1
	v_cmp_gt_u32_e64 s[10:11], 64, v0
	v_mov_b32_e32 v2, s50
	v_mov_b32_e32 v3, s51
	v_mov_b32_e32 v4, s54
	v_mov_b32_e32 v5, s55
	v_mov_b32_e32 v1, 0
	v_cmp_eq_u32_e32 vcc, 0, v0
	s_and_saveexec_b64 s[6:7], vcc
	ds_write_b128 v1, v[2:5] offset:16400

.LBB2_30:
	s_or_b64 exec, exec, s[0:1]
	v_mov_b32_e32 v4, 0
	s_mov_b64 s[0:1], s[24:25]
.Lrg_rank:
	s_ff1_i32_b64 s4, s[0:1]
	s_bitset0_b64 s[0:1], s4
	v_readlane_b32 s5, v1, s4
	v_cmp_gt_u32_e64 s[20:21], v26, s4
	s_nop 1
	v_cmp_eq_f32_e64 s[22:23], s5, v1
	v_cmp_gt_f32_e64 s[16:17], s5, v1
	s_and_b64 s[20:21], s[20:21], s[22:23]
	s_or_b64 s[16:17], s[16:17], s[20:21]
	v_addc_co_u32_e64 v4, vcc, 0, v4, s[16:17]
	s_cmp_lg_u64 s[0:1], 0
	s_cbranch_scc1 .Lrg_rank
	v_bcnt_u32_b32 v2, v2, 0
	v_bcnt_u32_b32 v2, v3, v2
	v_sub_u32_e32 v2, 32, v2
	v_cmp_lt_i32_e64 s[0:1], v4, v2
	s_and_b64 s[0:1], s[0:1], s[24:25]
	s_or_b64 s[10:11], s[10:11], s[0:1]
